# attention QK: K-fragment reads double-buffered through spare VGPRs so each read is issued one MFMA earlier (on top of merge-loop fix and unscaled fp8 MFMA)
# speedup vs baseline: 1.0110x; 1.0063x over previous
; __device__ __forceinline__ unsigned sel_bit_mask(unsigned w, int b) { unsigned m; asm("v_bfe_i32 %0, %1, %2, 1" : "=v"(m) : "v"(w), "n"(b)); return m; }
; template <bool SEL>
; __device__ __forceinline__ void finishSM(f32x16& p0, f32x16& p1, float alpha, float& l_reg, bf16x8& pa0, bf16x8& pa1, bf16x8& pa2, bf16x8& pa3, unsigned selw) {
; #pragma unroll
;     for (int r = 0; r < 16; ++r) p1[r] = __builtin_amdgcn_exp2f(p1[r]);
;     if (SEL) {
; #pragma unroll
;         for (int r = 0; r < 16; ++r) p1[r] = __uint_as_float(__float_as_uint(p1[r]) & sel_bit_mask(selw, 16 + r));
;     }
;     float ps = 0;
; #pragma unroll
;     for (int r = 0; r < 16; ++r) ps += p0[r];
; #pragma unroll
;     for (int r = 0; r < 16; ++r) ps += p1[r];
;     { auto rr = __builtin_amdgcn_permlane32_swap(__float_as_uint(ps), __float_as_uint(ps), false, false);
;       ps = __uint_as_float(rr[0]) + __uint_as_float(rr[1]); }
;     l_reg = l_reg * alpha + ps;
;     ...
;     PK4(p0, 0, pa0); PK4(p0, 8, pa1); PK4(p1, 0, pa2); PK4(p1, 8, pa3);
; template <int KB, int QREG>
; __device__ __forceinline__ void qkt(f32x16& p0, f32x16& p1, const char* K_lds, int r32, int hi, const bf16x8* qr, const char* qlds) {
;     p0 = f32x16{}; p1 = f32x16{};
;     const char* kb[4];
; #pragma unroll
;     for (int dd = 0; dd < 4; ++dd) kb[dd] = K_lds + KB * SHM_K + KSWZ(r32, (dd * 16 + hi * 8) * 2);
; #pragma unroll
;     for (int d0 = 0; d0 < 8; ++d0) { const char* a = kb[d0 & 3] + (d0 >> 2) * 128;
;         bf16x8 b0 = *reinterpret_cast<const bf16x8*>(a);
;         bf16x8 b1 = *reinterpret_cast<const bf16x8*>(a + 32 * 256);
;         const bf16x8 qf = (d0 < QREG) ? qr[d0 < QREG ? d0 : 0] : *reinterpret_cast<const bf16x8*>(qlds + (d0 - QREG) * 1024);
;         p0 = __builtin_amdgcn_mfma_f32_32x32x16_bf16(b0, qf, p0, 0, 0, 0);
;         p1 = __builtin_amdgcn_mfma_f32_32x32x16_bf16(b1, qf, p1, 0, 0, 0); }
.LBB0_1812:
	ds_read_b128 v[2:5], v213 offset:49152
	ds_read_b128 v[250:253], v212 offset:49152
	ds_read_b128 v[6:9], v213 offset:49280
	v_add_f32_e32 v0, 0, v126
	v_add_f32_e32 v0, v127, v0
	v_add_f32_e32 v0, v124, v0
	s_waitcnt lgkmcnt(2)
	v_mfma_f32_32x32x16_bf16 v[96:111], v[2:5], v[164:167], 0
	ds_read_b128 v[2:5], v213 offset:57344
	ds_read_b128 v[10:13], v212 offset:49280
	v_add_f32_e32 v0, v125, v0
	v_add_f32_e32 v0, v122, v0
	v_add_f32_e32 v0, v123, v0
	v_add_f32_e32 v0, v120, v0
	v_add_f32_e32 v0, v121, v0
	v_add_f32_e32 v0, v118, v0
	s_waitcnt lgkmcnt(3)
	v_mfma_f32_32x32x16_bf16 v[96:111], v[250:253], v[160:163], v[96:111]
	ds_read_b128 v[250:253], v212 offset:57344
	ds_read_b128 v[128:131], v213 offset:57472
	v_add_f32_e32 v0, v119, v0
	v_add_f32_e32 v0, v116, v0
	v_add_f32_e32 v0, v117, v0
	v_add_f32_e32 v0, v114, v0
	v_add_f32_e32 v0, v115, v0
	v_add_f32_e32 v0, v112, v0
	s_waitcnt lgkmcnt(3)
	v_mfma_f32_32x32x16_bf16 v[80:95], v[2:5], v[164:167], 0
	ds_read_b128 v[2:5], v211 offset:49152
	ds_read_b128 v[132:135], v212 offset:57472
	v_add_f32_e32 v0, v113, v0
	s_waitcnt lgkmcnt(3)
	v_mfma_f32_32x32x16_bf16 v[80:95], v[250:253], v[160:163], v[80:95]
	ds_read_b128 v[250:253], v211 offset:57344
	ds_read_b128 v[136:139], v211 offset:49280
	s_waitcnt lgkmcnt(3)
	v_mfma_f32_32x32x16_bf16 v[96:111], v[2:5], v[156:159], v[96:111]
	ds_read_b128 v[2:5], v210 offset:49152
	ds_read_b128 v[140:143], v211 offset:57472
	s_waitcnt lgkmcnt(3)
	v_mfma_f32_32x32x16_bf16 v[80:95], v[250:253], v[156:159], v[80:95]
	ds_read_b128 v[250:253], v210 offset:57344
	ds_read_b128 v[220:223], v210 offset:49280
	s_waitcnt lgkmcnt(3)
	v_mfma_f32_32x32x16_bf16 v[96:111], v[2:5], v[152:155], v[96:111]
	ds_read_b128 v[224:227], v210 offset:57472
	s_waitcnt lgkmcnt(2)
	v_mfma_f32_32x32x16_bf16 v[80:95], v[250:253], v[152:155], v[80:95]
	v_mfma_f32_32x32x16_bf16 v[96:111], v[6:9], v[148:151], v[96:111]
	ds_read_b128 v[2:5], v208
	ds_read_b128 v[6:9], v208 offset:1024
	v_cvt_pk_bf16_f32 v126, v126, v127
	v_cvt_pk_bf16_f32 v127, v124, v125
	v_exp_f32_e32 v124, v172
	v_exp_f32_e32 v125, v173
	v_mfma_f32_32x32x16_bf16 v[80:95], v[128:131], v[148:151], v[80:95]
	v_cvt_pk_bf16_f32 v128, v122, v123
	v_exp_f32_e32 v122, v174
	v_exp_f32_e32 v123, v175
	v_exp_f32_e32 v129, v170
	v_exp_f32_e32 v130, v171
	v_exp_f32_e32 v131, v168
	v_permlane32_swap_b32_e32 v126, v128
	v_mfma_f32_32x32x16_bf16 v[96:111], v[10:13], v[144:147], v[96:111]
	v_exp_f32_e32 v10, v178
	v_exp_f32_e32 v11, v179
	v_exp_f32_e32 v12, v176
	v_exp_f32_e32 v13, v177
	v_mfma_f32_32x32x16_bf16 v[80:95], v[132:135], v[144:147], v[80:95]
	v_bfe_i32 v133, v195, 16, 1
	v_exp_f32_e32 v132, v169
	s_waitcnt lgkmcnt(1)
	v_mfma_f32_32x32x16_bf16 v[96:111], v[136:139], v[2:5], v[96:111]
	v_mfma_f32_32x32x16_bf16 v[80:95], v[140:143], v[2:5], v[80:95]
	v_exp_f32_e32 v2, v182
	v_exp_f32_e32 v3, v183
	v_exp_f32_e32 v4, v180
	v_exp_f32_e32 v5, v181
	v_and_b32_e32 v2, v133, v2
	v_bfe_i32 v133, v195, 17, 1
	v_add_f32_e32 v0, v0, v2
	v_and_b32_e32 v3, v133, v3
	v_bfe_i32 v133, v195, 18, 1
	v_add_f32_e32 v0, v0, v3
	v_and_b32_e32 v4, v133, v4
	v_bfe_i32 v133, v195, 19, 1
	v_add_f32_e32 v0, v0, v4
	v_and_b32_e32 v5, v133, v5
	v_bfe_i32 v133, v195, 20, 1
	v_add_f32_e32 v0, v0, v5
	v_and_b32_e32 v10, v133, v10
	v_bfe_i32 v133, v195, 21, 1
	v_add_f32_e32 v0, v0, v10
	v_and_b32_e32 v11, v133, v11
	v_bfe_i32 v133, v195, 22, 1
	v_add_f32_e32 v0, v0, v11
	v_and_b32_e32 v12, v133, v12
	v_bfe_i32 v133, v195, 23, 1
	v_add_f32_e32 v0, v0, v12
	v_and_b32_e32 v13, v133, v13
	v_bfe_i32 v133, v195, 24, 1
	v_add_f32_e32 v0, v0, v13
	v_and_b32_e32 v122, v133, v122
	v_bfe_i32 v133, v195, 25, 1
	v_add_f32_e32 v0, v0, v122
	v_and_b32_e32 v123, v133, v123
	v_bfe_i32 v133, v195, 26, 1
	v_add_f32_e32 v0, v0, v123
	v_and_b32_e32 v124, v133, v124
	v_bfe_i32 v133, v195, 27, 1
	s_waitcnt lgkmcnt(0)
	v_mfma_f32_32x32x16_bf16 v[96:111], v[220:223], v[6:9], v[96:111]
	v_and_b32_e32 v125, v133, v125
	v_bfe_i32 v133, v195, 28, 1
	v_add_f32_e32 v0, v0, v124
	v_and_b32_e32 v133, v133, v129
	v_add_f32_e32 v0, v0, v125
	v_bfe_i32 v129, v195, 29, 1
	v_add_f32_e32 v0, v0, v133
	v_mfma_f32_32x32x16_bf16 v[80:95], v[224:227], v[6:9], v[80:95]
	v_and_b32_e32 v130, v129, v130
	v_bfe_i32 v129, v195, 30, 1
	v_add_f32_e32 v0, v0, v130
	v_and_b32_e32 v131, v129, v131
	v_bfe_i32 v129, v195, 31, 1
	v_add_f32_e32 v0, v0, v131
	v_and_b32_e32 v132, v129, v132
	v_add_f32_e32 v189, v0, v132
	v_mov_b32_e32 v219, v189
	v_cvt_pk_bf16_f32 v129, v120, v121
	v_cvt_pk_bf16_f32 v118, v118, v119
	v_cvt_pk_bf16_f32 v119, v116, v117
	v_cvt_pk_bf16_f32 v120, v114, v115
	v_cvt_pk_bf16_f32 v121, v112, v113
	v_cvt_pk_bf16_f32 v112, v2, v3
	v_cvt_pk_bf16_f32 v113, v4, v5
	v_cvt_pk_bf16_f32 v114, v10, v11
	v_cvt_pk_bf16_f32 v115, v12, v13
	v_cvt_pk_bf16_f32 v122, v122, v123
	v_cvt_pk_bf16_f32 v123, v124, v125
	v_cvt_pk_bf16_f32 v124, v133, v130
	v_cvt_pk_bf16_f32 v125, v131, v132
	s_nop 1
	v_permlane32_swap_b32_e32 v189, v219
	v_permlane32_swap_b32_e32 v127, v129
	v_permlane32_swap_b32_e32 v118, v120
	v_permlane32_swap_b32_e32 v119, v121
	v_permlane32_swap_b32_e32 v112, v114
	v_permlane32_swap_b32_e32 v113, v115
	v_permlane32_swap_b32_e32 v122, v124
	v_permlane32_swap_b32_e32 v123, v125
	v_add_u32_e32 v4, 32, v196
	v_add_u32_e32 v0, -2, v194
	v_ashrrev_i32_e32 v197, 31, v196
	v_ashrrev_i32_e32 v5, 31, v4
	v_lshl_add_u64 v[2:3], v[0:1], 2, s[44:45]
	v_lshlrev_b64 v[10:11], 10, v[196:197]
	v_lshlrev_b64 v[12:13], 10, v[4:5]
	global_load_dword v217, v[2:3], off
	v_lshl_add_u64 v[2:3], v[14:15], 0, v[10:11]
	v_lshl_add_u64 v[6:7], v[14:15], 0, v[12:13]
	v_lshl_add_u64 v[10:11], v[192:193], 0, v[10:11]
	global_load_dwordx4 v[2:5], v[2:3], off
	s_nop 0
	global_load_dwordx4 v[6:9], v[6:7], off
	v_lshl_add_u64 v[116:117], v[192:193], 0, v[12:13]
	global_load_dwordx4 v[10:13], v[10:11], off
	s_nop 0
	global_load_dwordx4 v[168:171], v[116:117], off
	ds_read_b64_tr_b16 v[130:131], v206 offset:0
	ds_read_b64_tr_b16 v[132:133], v206 offset:0x800
	ds_read_b64_tr_b16 v[134:135], v206 offset:0x1000
	ds_read_b64_tr_b16 v[136:137], v206 offset:0x1800
	ds_read_b64_tr_b16 v[138:139], v206 offset:0x2000
	ds_read_b64_tr_b16 v[140:141], v206 offset:0x2800
	ds_read_b64_tr_b16 v[172:173], v206 offset:0x3000
	ds_read_b64_tr_b16 v[174:175], v206 offset:0x3800
	s_waitcnt lgkmcnt(0)
; template <bool SEL>
; __device__ __forceinline__ void partialSM(f32x16& p0, f32x16& p1, float& m_reg, float& mn, float& alpha, unsigned selw) {
;     float pmax = p0[0];
; #pragma unroll
;     for (int r = 1; r < 16; ++r) pmax = fmaxf(pmax, p0[r]);
; #pragma unroll
;     for (int r = 0; r < 16; ++r) pmax = fmaxf(pmax, p1[r]);
;     { auto rr = __builtin_amdgcn_permlane32_swap(__float_as_uint(pmax), __float_as_uint(pmax), false, false);
;       pmax = fmaxf(__uint_as_float(rr[0]), __uint_as_float(rr[1])); }
;     constexpr float C2 = 1.4426950408889634f * SCALE;
;     if (__builtin_expect(__all((pmax - m_reg) * SCALE <= THR), 1)) { mn = m_reg; alpha = 1.f; }
;     else { mn = fmaxf(m_reg, pmax); alpha = __builtin_amdgcn_exp2f((m_reg - mn) * C2); m_reg = mn; }
;     const float mnL = -mn * C2;
; #pragma unroll
; template <int VB>
; __device__ __forceinline__ void pv_tile(f32x16* o, int vb0, bf16x8 pa0, bf16x8 pa1, bf16x8 pa2, bf16x8 pa3) {
;     ...
;     PV_D0(0); PV_D0(1); PV_D0(2); PV_D0(3);
;     ...
; }
	s_nop 0
	v_mfma_f32_32x32x16_bf16 v[64:79], v[126:129], v[130:133], v[64:79]
	ds_read_b64_tr_b16 v[130:131], v206 offset:0x200
	ds_read_b64_tr_b16 v[132:133], v206 offset:0xa00
	v_mfma_f32_32x32x16_bf16 v[64:79], v[118:121], v[134:137], v[64:79]
	ds_read_b64_tr_b16 v[134:135], v206 offset:0x1200
	ds_read_b64_tr_b16 v[136:137], v206 offset:0x1a00
	v_mfma_f32_32x32x16_bf16 v[64:79], v[112:115], v[138:141], v[64:79]
	ds_read_b64_tr_b16 v[138:139], v206 offset:0x2200
	ds_read_b64_tr_b16 v[140:141], v206 offset:0x2a00
	ds_read_b64_tr_b16 v[176:177], v206 offset:0x3200
	ds_read_b64_tr_b16 v[178:179], v206 offset:0x3a00
	s_waitcnt lgkmcnt(0)
	v_mfma_f32_32x32x16_bf16 v[64:79], v[122:125], v[172:175], v[64:79]
	v_mfma_f32_32x32x16_bf16 v[48:63], v[126:129], v[130:133], v[48:63]
	ds_read_b64_tr_b16 v[130:131], v206 offset:0x400
	ds_read_b64_tr_b16 v[132:133], v206 offset:0xc00
	v_mfma_f32_32x32x16_bf16 v[48:63], v[118:121], v[134:137], v[48:63]
	ds_read_b64_tr_b16 v[134:135], v206 offset:0x1400
	ds_read_b64_tr_b16 v[136:137], v206 offset:0x1c00
	v_mfma_f32_32x32x16_bf16 v[48:63], v[112:115], v[138:141], v[48:63]
	ds_read_b64_tr_b16 v[138:139], v206 offset:0x2400
	ds_read_b64_tr_b16 v[140:141], v206 offset:0x2c00
	ds_read_b64_tr_b16 v[172:173], v206 offset:0x3400
	ds_read_b64_tr_b16 v[174:175], v206 offset:0x3c00
	s_waitcnt lgkmcnt(0)
	v_mfma_f32_32x32x16_bf16 v[48:63], v[122:125], v[176:179], v[48:63]
	v_mfma_f32_32x32x16_bf16 v[32:47], v[126:129], v[130:133], v[32:47]
	ds_read_b64_tr_b16 v[130:131], v206 offset:0x600
	ds_read_b64_tr_b16 v[132:133], v206 offset:0xe00
	v_mfma_f32_32x32x16_bf16 v[32:47], v[118:121], v[134:137], v[32:47]
	ds_read_b64_tr_b16 v[134:135], v206 offset:0x1600
	ds_read_b64_tr_b16 v[136:137], v206 offset:0x1e00
	v_mfma_f32_32x32x16_bf16 v[32:47], v[112:115], v[138:141], v[32:47]
	ds_read_b64_tr_b16 v[138:139], v206 offset:0x2600
	ds_read_b64_tr_b16 v[140:141], v206 offset:0x2e00
	ds_read_b64_tr_b16 v[176:177], v206 offset:0x3600
	ds_read_b64_tr_b16 v[178:179], v206 offset:0x3e00
	s_waitcnt lgkmcnt(0)
	v_mfma_f32_32x32x16_bf16 v[32:47], v[122:125], v[172:175], v[32:47]
	v_mfma_f32_32x32x16_bf16 v[16:31], v[126:129], v[130:133], v[16:31]
	v_max_f32_e32 v0, v97, v97
	s_barrier
	s_waitcnt vmcnt(0)
	s_waitcnt vmcnt(4)
	v_bfe_i32 v116, v217, 8, 1
	v_bfe_i32 v117, v217, 10, 1
	v_mfma_f32_32x32x16_bf16 v[16:31], v[118:121], v[134:137], v[16:31]
	v_bfe_i32 v120, v217, 1, 1
	v_bfe_i32 v121, v217, 3, 1
	v_bfe_i32 v118, v217, 12, 1
	v_bfe_i32 v126, v217, 13, 1
	v_bfe_i32 v119, v217, 14, 1
	v_bfe_i32 v127, v217, 15, 1
	s_waitcnt vmcnt(3)
	ds_write_b128 v216, v[2:5]
	s_waitcnt vmcnt(2)
	ds_write_b128 v218, v[6:9]
	s_waitcnt vmcnt(1)
	ds_write_b128 v204, v[10:13] offset:32768
	s_waitcnt vmcnt(0)
	ds_write_b128 v204, v[168:171] offset:40960
	v_mfma_f32_32x32x16_bf16 v[16:31], v[112:115], v[138:141], v[16:31]
	v_max_f32_e32 v112, v96, v96
	v_max_f32_e32 v0, v112, v0
	v_max3_f32 v0, v0, v98, v99
	v_max3_f32 v0, v0, v100, v101
	v_max3_f32 v0, v0, v102, v103
	v_max3_f32 v0, v0, v104, v105
	v_max3_f32 v0, v0, v106, v107
	v_max3_f32 v0, v0, v108, v109
	v_max3_f32 v0, v0, v110, v111
	v_max3_f32 v0, v0, v80, v81
	v_max3_f32 v0, v0, v82, v83
	v_max3_f32 v0, v0, v84, v85
	v_max3_f32 v0, v0, v86, v87
	v_max3_f32 v0, v0, v88, v89
	v_max3_f32 v0, v0, v90, v91
	v_max3_f32 v0, v0, v92, v93
	v_max3_f32 v0, v0, v94, v95
	v_mov_b32_e32 v112, v0
	s_nop 1
	v_permlane32_swap_b32_e32 v0, v112
	v_max_f32_e32 v112, v112, v112
	v_max_f32_e32 v0, v0, v0
	v_max_f32_e32 v0, v0, v112
	v_sub_f32_e32 v112, v0, v184
	v_mul_f32_e32 v112, 0x3db504f3, v112
	v_cmp_ge_f32_e32 vcc, s5, v112
	v_max_f32_e32 v112, v184, v184
	v_max_f32_e32 v128, v112, v0
	v_mfma_f32_32x32x16_bf16 v[16:31], v[122:125], v[176:179], v[16:31]
	v_sub_f32_e32 v0, v184, v128
	v_mul_f32_e32 v0, 0x3e0293ee, v0
	v_exp_f32_e32 v0, v0
	s_cmp_eq_u64 vcc, exec
	s_cselect_b64 s[2:3], -1, 0
	v_bfe_i32 v112, v217, 0, 1
	v_cndmask_b32_e64 v0, v0, 1.0, s[2:3]
	v_cmp_gt_f32_e32 vcc, 1.0, v0
	v_bfe_i32 v113, v217, 2, 1
	v_bfe_i32 v114, v217, 4, 1
	v_bfe_i32 v122, v217, 5, 1
	v_bfe_i32 v115, v217, 6, 1
	v_bfe_i32 v123, v217, 7, 1
	v_bfe_i32 v124, v217, 9, 1
	v_bfe_i32 v125, v217, 11, 1
	s_cbranch_vccz .LBB0_1816
	s_and_saveexec_b64 s[48:49], s[0:1]
	ds_write_b32 v205, v0 offset:128
	s_or_b64 exec, exec, s[48:49]
	s_waitcnt lgkmcnt(0)
	v_add_u32_e32 v129, s66, v203
	ds_read_b128 v[130:133], v129 offset:224
	ds_read_b128 v[134:137], v129 offset:192
	ds_read_b128 v[138:141], v129 offset:160
	ds_read_b128 v[172:175], v129 offset:128
	s_waitcnt lgkmcnt(3)
	v_pk_mul_f32 v[76:77], v[76:77], v[130:131]
	s_waitcnt lgkmcnt(2)
	v_pk_mul_f32 v[72:73], v[72:73], v[134:135]
	s_waitcnt lgkmcnt(1)
	v_pk_mul_f32 v[68:69], v[68:69], v[138:139]
	v_pk_mul_f32 v[78:79], v[78:79], v[132:133]
	v_pk_mul_f32 v[74:75], v[74:75], v[136:137]
	v_pk_mul_f32 v[70:71], v[70:71], v[140:141]
	s_waitcnt lgkmcnt(0)
	v_pk_mul_f32 v[66:67], v[66:67], v[174:175]
	v_pk_mul_f32 v[64:65], v[64:65], v[172:173]
	v_pk_mul_f32 v[60:61], v[60:61], v[130:131]
	v_pk_mul_f32 v[56:57], v[56:57], v[134:135]
	v_pk_mul_f32 v[52:53], v[52:53], v[138:139]
	v_pk_mul_f32 v[62:63], v[62:63], v[132:133]
	v_pk_mul_f32 v[58:59], v[58:59], v[136:137]
	v_pk_mul_f32 v[54:55], v[54:55], v[140:141]
	v_pk_mul_f32 v[50:51], v[50:51], v[174:175]
	v_pk_mul_f32 v[48:49], v[48:49], v[172:173]
	v_pk_mul_f32 v[44:45], v[44:45], v[130:131]
	v_pk_mul_f32 v[40:41], v[40:41], v[134:135]
	v_pk_mul_f32 v[36:37], v[36:37], v[138:139]
	v_pk_mul_f32 v[46:47], v[46:47], v[132:133]
	v_pk_mul_f32 v[42:43], v[42:43], v[136:137]
	v_pk_mul_f32 v[38:39], v[38:39], v[140:141]
	v_pk_mul_f32 v[34:35], v[34:35], v[174:175]
	v_pk_mul_f32 v[32:33], v[32:33], v[172:173]
	v_pk_mul_f32 v[28:29], v[28:29], v[130:131]
	v_pk_mul_f32 v[24:25], v[24:25], v[134:135]
	v_pk_mul_f32 v[20:21], v[20:21], v[138:139]
	v_pk_mul_f32 v[30:31], v[30:31], v[132:133]
	v_pk_mul_f32 v[26:27], v[26:27], v[136:137]
	v_pk_mul_f32 v[22:23], v[22:23], v[140:141]
	v_pk_mul_f32 v[18:19], v[18:19], v[174:175]
	v_pk_mul_f32 v[16:17], v[16:17], v[172:173]

; #define LAS __attribute__((address_space(3)))
; __global__ void __launch_bounds__(512, 2) fwd_kernel(Args args) {
;     extern __shared__ __attribute__((aligned(16))) unsigned char lds_raw[];
;     Frame F; F.a = &args; F.ws = args.ws; F.lds = (LAS unsigned char*)lds_raw;
;     F.wave = __builtin_amdgcn_readfirstlane(threadIdx.x >> 6); F.G = gridDim.x; F.bid = blockIdx.x;
	.amdhsa_kernel _Z10fwd_kernel4Args
		.amdhsa_group_segment_fixed_size 0
		.amdhsa_private_segment_fixed_size 0
		.amdhsa_kernarg_size 448
		.amdhsa_user_sgpr_count 2
		.amdhsa_user_sgpr_dispatch_ptr 0
		.amdhsa_user_sgpr_queue_ptr 0
		.amdhsa_user_sgpr_kernarg_segment_ptr 1
		.amdhsa_user_sgpr_dispatch_id 0
		.amdhsa_user_sgpr_kernarg_preload_length 0
		.amdhsa_user_sgpr_kernarg_preload_offset 0
		.amdhsa_user_sgpr_private_segment_size 0
		.amdhsa_uses_dynamic_stack 0
		.amdhsa_enable_private_segment 0
		.amdhsa_system_sgpr_workgroup_id_x 1
		.amdhsa_system_sgpr_workgroup_id_y 0
		.amdhsa_system_sgpr_workgroup_id_z 0
		.amdhsa_system_sgpr_workgroup_info 0
		.amdhsa_system_vgpr_workitem_id 0
		.amdhsa_next_free_vgpr 256
		.amdhsa_next_free_sgpr 98
		.amdhsa_accum_offset 256
		.amdhsa_reserve_vcc 1
		.amdhsa_float_round_mode_32 0
		.amdhsa_float_round_mode_16_64 0
		.amdhsa_float_denorm_mode_32 3
		.amdhsa_float_denorm_mode_16_64 3
		.amdhsa_dx10_clamp 1
		.amdhsa_ieee_mode 1
		.amdhsa_fp16_overflow 0
		.amdhsa_tg_split 0
		.amdhsa_exception_fp_ieee_invalid_op 0
		.amdhsa_exception_fp_denorm_src 0
		.amdhsa_exception_fp_ieee_div_zero 0
		.amdhsa_exception_fp_ieee_overflow 0
		.amdhsa_exception_fp_ieee_underflow 0
		.amdhsa_exception_fp_ieee_inexact 0
		.amdhsa_exception_int_div_zero 0
	.end_amdhsa_kernel

; #define LAS __attribute__((address_space(3)))
; __global__ void __launch_bounds__(512, 2) fwd_kernel(Args args) {
;     extern __shared__ __attribute__((aligned(16))) unsigned char lds_raw[];
;     Frame F; F.a = &args; F.ws = args.ws; F.lds = (LAS unsigned char*)lds_raw;
;     F.wave = __builtin_amdgcn_readfirstlane(threadIdx.x >> 6); F.G = gridDim.x; F.bid = blockIdx.x;
amdhsa.kernels:
  - .agpr_count:     0
    .args:
      - .offset:         0
        .size:           192
        .value_kind:     by_value
      - .offset:         192
        .size:           4
        .value_kind:     hidden_block_count_x
      - .offset:         196
        .size:           4
        .value_kind:     hidden_block_count_y
      - .offset:         200
        .size:           4
        .value_kind:     hidden_block_count_z
      - .offset:         204
        .size:           2
        .value_kind:     hidden_group_size_x
      - .offset:         206
        .size:           2
        .value_kind:     hidden_group_size_y
      - .offset:         208
        .size:           2
        .value_kind:     hidden_group_size_z
      - .offset:         210
        .size:           2
        .value_kind:     hidden_remainder_x
      - .offset:         212
        .size:           2
        .value_kind:     hidden_remainder_y
      - .offset:         214
        .size:           2
        .value_kind:     hidden_remainder_z
      - .offset:         232
        .size:           8
        .value_kind:     hidden_global_offset_x
      - .offset:         240
        .size:           8
        .value_kind:     hidden_global_offset_y
      - .offset:         248
        .size:           8
        .value_kind:     hidden_global_offset_z
      - .offset:         256
        .size:           2
        .value_kind:     hidden_grid_dims
      - .offset:         312
        .size:           4
        .value_kind:     hidden_dynamic_lds_size
    .group_segment_fixed_size: 0
    .kernarg_segment_align: 8
    .kernarg_segment_size: 448
    .language:       OpenCL C
    .language_version:
      - 2
      - 0
    .max_flat_workgroup_size: 512
    .name:           _Z10fwd_kernel4Args
    .private_segment_fixed_size: 0
    .sgpr_count:     104
    .sgpr_spill_count: 103
    .symbol:         _Z10fwd_kernel4Args.kd
    .uniform_work_group_size: 1
    .uses_dynamic_stack: false
    .vgpr_count:     256
    .vgpr_spill_count: 0
    .wavefront_size: 64
